# DSA pass 1 software-pipelined across tiles: score/histogram VALU of a tile's last two sub-tiles carried under the next tile's first 16 MFMAs (flushed before the diagonal tile); on top of v26
# speedup vs baseline: 1.0055x; 1.0055x over previous
.LBB0_497:
	s_or_b64 exec, exec, s[0:1]
	s_mul_i32 s0, s44, 0x1200000
	s_mul_hi_i32 s1, s44, 0x1200000
	s_add_u32 s0, s74, s0
	s_addc_u32 s1, s75, s1
	s_add_i32 s12, 0, 0x23400
	v_ashrrev_i32_e32 v54, 4, v42
	v_mov_b32_e32 v0, s12
	s_lshl_b32 s49, s30, 6
	v_readlane_b32 s13, v252, 19
	v_and_b32_e32 v232, 15, v42
	s_waitcnt lgkmcnt(0)
	s_barrier
	ds_read_b128 v[6:9], v0
	ds_read_b128 v[2:5], v0 offset:16
	s_or_b32 s12, s49, s13
	v_mov_b32_e32 v0, v54
	v_or_b32_e32 v44, s12, v232
	v_mov_b64_e32 v[10:11], s[0:1]
	v_lshlrev_b32_e32 v12, 3, v0
	v_mad_i64_i32 v[10:11], s[0:1], v44, s2, v[10:11]
	v_ashrrev_i32_e32 v13, 31, v12
	v_lshl_add_u64 v[38:39], v[12:13], 1, v[10:11]
	global_load_dwordx4 v[10:13], v[38:39], off offset:2048
	global_load_dwordx4 v[14:17], v[38:39], off offset:2112
	v_ashrrev_i32_e32 v45, 31, v44
	v_lshlrev_b64 v[18:19], 9, v[44:45]
	v_lshl_add_u64 v[18:19], s[42:43], 0, v[18:19]
	global_load_dwordx2 v[50:51], v[18:19], off offset:384
	global_load_dwordx4 v[72:75], v[38:39], off offset:2048
	global_load_dwordx4 v[76:79], v[38:39], off offset:2112
	global_load_dwordx4 v[80:83], v[38:39], off offset:2176
	global_load_dwordx4 v[84:87], v[38:39], off offset:2240
	global_load_dwordx4 v[88:91], v[38:39], off offset:2304
	global_load_dwordx4 v[92:95], v[38:39], off offset:2368
	global_load_dwordx4 v[96:99], v[38:39], off offset:2432
	global_load_dwordx4 v[100:103], v[38:39], off offset:2496
	v_ashrrev_i32_e32 v233, 3, v42
	v_readlane_b32 s12, v251, 50
	s_add_u32 s0, s42, 0x100
	s_addc_u32 s1, s43, 0
	v_add_u32_e32 v46, s12, v233
	v_ashrrev_i32_e32 v47, 31, v46
	v_lshlrev_b64 v[46:47], 9, v[46:47]
	s_movk_i32 s12, 0x70
	s_mov_b64 s[16:17], 0x8000
	s_add_i32 s30, s30, 2
	s_ashr_i32 s50, s30, 1
	v_ashrrev_i32_e32 v43, 31, v42
	s_waitcnt vmcnt(2)
	v_lshlrev_b32_e32 v0, 16, v10
	v_and_b32_e32 v10, 0xffff0000, v10
	v_lshlrev_b32_e32 v18, 16, v11
	v_and_b32_e32 v11, 0xffff0000, v11
	v_lshlrev_b32_e32 v19, 16, v12
	v_and_b32_e32 v12, 0xffff0000, v12
	v_mul_f32_e32 v10, v10, v10
	v_mul_f32_e32 v11, v11, v11
	v_lshlrev_b32_e32 v20, 16, v13
	v_and_b32_e32 v13, 0xffff0000, v13
	v_mul_f32_e32 v12, v12, v12
	v_fmac_f32_e32 v10, v0, v0
	v_fmac_f32_e32 v11, v18, v18
	s_waitcnt vmcnt(1)
	v_lshlrev_b32_e32 v21, 16, v14
	v_and_b32_e32 v14, 0xffff0000, v14
	v_mul_f32_e32 v13, v13, v13
	v_fmac_f32_e32 v12, v19, v19
	v_add_f32_e32 v0, v10, v11
	v_lshlrev_b32_e32 v22, 16, v15
	v_and_b32_e32 v15, 0xffff0000, v15
	v_mul_f32_e32 v14, v14, v14
	v_fmac_f32_e32 v13, v20, v20
	v_add_f32_e32 v0, v12, v0
	v_lshlrev_b32_e32 v23, 16, v16
	v_and_b32_e32 v16, 0xffff0000, v16
	v_mul_f32_e32 v15, v15, v15
	v_fmac_f32_e32 v14, v21, v21
	v_add_f32_e32 v0, v13, v0
	v_lshlrev_b32_e32 v24, 16, v17
	v_and_b32_e32 v17, 0xffff0000, v17
	v_mul_f32_e32 v16, v16, v16
	v_fmac_f32_e32 v15, v22, v22
	v_add_f32_e32 v0, v14, v0
	v_mul_f32_e32 v17, v17, v17
	v_fmac_f32_e32 v16, v23, v23
	v_add_f32_e32 v0, v15, v0
	v_fmac_f32_e32 v17, v24, v24
	v_add_f32_e32 v0, v16, v0
	v_add_f32_e32 v0, v17, v0
	v_mov_b32_e32 v10, v0
	s_nop 1
	v_permlane16_swap_b32_e32 v0, v10
	v_add_f32_e32 v56, v0, v10
	v_mov_b32_e32 v57, v56
	v_mov_b64_e32 v[10:11], v[80:81]
	v_mov_b64_e32 v[12:13], v[82:83]
	v_mov_b64_e32 v[14:15], v[84:85]
	v_mov_b64_e32 v[16:17], v[86:87]
	v_permlane32_swap_b32_e32 v56, v57
	s_waitcnt vmcnt(1)
	v_lshlrev_b32_e32 v0, 16, v10
	v_and_b32_e32 v10, 0xffff0000, v10
	v_lshlrev_b32_e32 v18, 16, v11
	v_and_b32_e32 v11, 0xffff0000, v11
	v_lshlrev_b32_e32 v19, 16, v12
	v_and_b32_e32 v12, 0xffff0000, v12
	v_mul_f32_e32 v10, v10, v10
	v_mul_f32_e32 v11, v11, v11
	v_lshlrev_b32_e32 v20, 16, v13
	v_and_b32_e32 v13, 0xffff0000, v13
	v_mul_f32_e32 v12, v12, v12
	v_fmac_f32_e32 v10, v0, v0
	v_fmac_f32_e32 v11, v18, v18
	s_waitcnt vmcnt(0)
	v_lshlrev_b32_e32 v21, 16, v14
	v_and_b32_e32 v14, 0xffff0000, v14
	v_mul_f32_e32 v13, v13, v13
	v_fmac_f32_e32 v12, v19, v19
	v_add_f32_e32 v0, v10, v11
	v_lshlrev_b32_e32 v22, 16, v15
	v_and_b32_e32 v15, 0xffff0000, v15
	v_mul_f32_e32 v14, v14, v14
	v_fmac_f32_e32 v13, v20, v20
	v_add_f32_e32 v0, v12, v0
	v_lshlrev_b32_e32 v23, 16, v16
	v_and_b32_e32 v16, 0xffff0000, v16
	v_mul_f32_e32 v15, v15, v15
	v_fmac_f32_e32 v14, v21, v21
	v_add_f32_e32 v0, v13, v0
	v_lshlrev_b32_e32 v24, 16, v17
	v_and_b32_e32 v17, 0xffff0000, v17
	v_mul_f32_e32 v16, v16, v16
	v_fmac_f32_e32 v15, v22, v22
	v_add_f32_e32 v0, v14, v0
	v_mul_f32_e32 v17, v17, v17
	v_fmac_f32_e32 v16, v23, v23
	v_add_f32_e32 v0, v15, v0
	v_fmac_f32_e32 v17, v24, v24
	v_add_f32_e32 v0, v16, v0
	v_add_f32_e32 v0, v17, v0
	v_mov_b32_e32 v10, v0
	s_nop 1
	v_permlane16_swap_b32_e32 v0, v10
	v_add_f32_e32 v58, v0, v10
	v_mov_b32_e32 v59, v58
	v_mov_b64_e32 v[10:11], v[88:89]
	v_mov_b64_e32 v[12:13], v[90:91]
	v_mov_b64_e32 v[14:15], v[92:93]
	v_mov_b64_e32 v[16:17], v[94:95]
	v_permlane32_swap_b32_e32 v58, v59
	s_waitcnt vmcnt(1)
	v_lshlrev_b32_e32 v0, 16, v10
	v_and_b32_e32 v10, 0xffff0000, v10
	v_lshlrev_b32_e32 v18, 16, v11
	v_and_b32_e32 v11, 0xffff0000, v11
	v_lshlrev_b32_e32 v19, 16, v12
	v_and_b32_e32 v12, 0xffff0000, v12
	v_mul_f32_e32 v10, v10, v10
	v_mul_f32_e32 v11, v11, v11
	v_lshlrev_b32_e32 v20, 16, v13
	v_and_b32_e32 v13, 0xffff0000, v13
	v_mul_f32_e32 v12, v12, v12
	v_fmac_f32_e32 v10, v0, v0
	v_fmac_f32_e32 v11, v18, v18
	s_waitcnt vmcnt(0)
	v_lshlrev_b32_e32 v21, 16, v14
	v_and_b32_e32 v14, 0xffff0000, v14
	v_mul_f32_e32 v13, v13, v13
	v_fmac_f32_e32 v12, v19, v19
	v_add_f32_e32 v0, v10, v11
	v_lshlrev_b32_e32 v22, 16, v15
	v_and_b32_e32 v15, 0xffff0000, v15
	v_mul_f32_e32 v14, v14, v14
	v_fmac_f32_e32 v13, v20, v20
	v_add_f32_e32 v0, v12, v0
	v_lshlrev_b32_e32 v23, 16, v16
	v_and_b32_e32 v16, 0xffff0000, v16
	v_mul_f32_e32 v15, v15, v15
	v_fmac_f32_e32 v14, v21, v21
	v_add_f32_e32 v0, v13, v0
	v_lshlrev_b32_e32 v24, 16, v17
	v_and_b32_e32 v17, 0xffff0000, v17
	v_mul_f32_e32 v16, v16, v16
	v_fmac_f32_e32 v15, v22, v22
	v_add_f32_e32 v0, v14, v0
	v_mul_f32_e32 v17, v17, v17
	v_fmac_f32_e32 v16, v23, v23
	v_add_f32_e32 v0, v15, v0
	v_fmac_f32_e32 v17, v24, v24
	v_add_f32_e32 v0, v16, v0
	v_add_f32_e32 v0, v17, v0
	v_mov_b32_e32 v10, v0
	s_nop 1
	v_permlane16_swap_b32_e32 v0, v10
	v_add_f32_e32 v60, v0, v10
	v_mov_b32_e32 v61, v60
	v_mov_b64_e32 v[10:11], v[96:97]
	v_mov_b64_e32 v[12:13], v[98:99]
	v_mov_b64_e32 v[14:15], v[100:101]
	v_mov_b64_e32 v[16:17], v[102:103]
	v_permlane32_swap_b32_e32 v60, v61
	s_waitcnt vmcnt(1)
	v_lshlrev_b32_e32 v0, 16, v10
	v_and_b32_e32 v10, 0xffff0000, v10
	v_lshlrev_b32_e32 v18, 16, v11
	v_and_b32_e32 v11, 0xffff0000, v11
	v_lshlrev_b32_e32 v19, 16, v12
	v_and_b32_e32 v12, 0xffff0000, v12
	v_mul_f32_e32 v10, v10, v10
	v_mul_f32_e32 v11, v11, v11
	v_lshlrev_b32_e32 v20, 16, v13
	v_and_b32_e32 v13, 0xffff0000, v13
	v_mul_f32_e32 v12, v12, v12
	v_fmac_f32_e32 v10, v0, v0
	v_fmac_f32_e32 v11, v18, v18
	s_waitcnt vmcnt(0)
	v_lshlrev_b32_e32 v21, 16, v14
	v_and_b32_e32 v14, 0xffff0000, v14
	v_mul_f32_e32 v13, v13, v13
	v_fmac_f32_e32 v12, v19, v19
	v_add_f32_e32 v0, v10, v11
	v_lshlrev_b32_e32 v22, 16, v15
	v_and_b32_e32 v15, 0xffff0000, v15
	v_mul_f32_e32 v14, v14, v14
	v_fmac_f32_e32 v13, v20, v20
	v_add_f32_e32 v0, v12, v0
	v_lshlrev_b32_e32 v23, 16, v16
	v_and_b32_e32 v16, 0xffff0000, v16
	v_mul_f32_e32 v15, v15, v15
	v_fmac_f32_e32 v14, v21, v21
	v_add_f32_e32 v0, v13, v0
	v_lshlrev_b32_e32 v24, 16, v17
	v_and_b32_e32 v17, 0xffff0000, v17
	v_mul_f32_e32 v16, v16, v16
	v_fmac_f32_e32 v15, v22, v22
	v_add_f32_e32 v0, v14, v0
	v_mul_f32_e32 v17, v17, v17
	v_fmac_f32_e32 v16, v23, v23
	v_add_f32_e32 v0, v15, v0
	v_fmac_f32_e32 v17, v24, v24
	v_add_f32_e32 v0, v16, v0
	v_add_f32_e32 v0, v17, v0
	v_mov_b32_e32 v10, v0
	s_nop 1
	v_permlane16_swap_b32_e32 v0, v10
	v_add_f32_e32 v62, v0, v10
	v_mov_b32_e32 v63, v62
	v_mov_b64_e32 v[30:31], v[72:73]
	v_mov_b64_e32 v[32:33], v[74:75]
	v_mov_b64_e32 v[26:27], v[76:77]
	v_mov_b64_e32 v[28:29], v[78:79]
	v_mov_b64_e32 v[22:23], v[80:81]
	v_mov_b64_e32 v[24:25], v[82:83]
	v_mov_b64_e32 v[18:19], v[84:85]
	v_mov_b64_e32 v[20:21], v[86:87]
	v_mov_b64_e32 v[14:15], v[88:89]
	v_mov_b64_e32 v[16:17], v[90:91]
	v_mov_b64_e32 v[10:11], v[92:93]
	v_mov_b64_e32 v[12:13], v[94:95]
	v_mov_b64_e32 v[34:35], v[96:97]
	v_mov_b64_e32 v[36:37], v[98:99]
	s_nop 0
	v_mov_b64_e32 v[38:39], v[100:101]
	v_mov_b64_e32 v[40:41], v[102:103]
	v_xor_b32_e32 v0, v233, v42
	v_lshlrev_b32_e32 v0, 4, v0
	v_and_or_b32 v46, v0, s12, v46
	v_lshl_add_u64 v[48:49], v[46:47], 0, s[16:17]
	v_lshl_add_u64 v[64:65], s[0:1], 0, v[46:47]
	s_mov_b32 s12, m0
	s_mov_b32 m0, s93
	s_nop 0
	global_load_lds_dwordx4 v[64:65], off
	s_mov_b32 m0, s12
	v_lshl_add_u64 v[64:65], s[0:1], 0, v[48:49]
	s_add_i32 s0, s93, 0x2000
	s_mov_b32 s1, m0
	s_mov_b32 m0, s0
	s_nop 0
	global_load_lds_dwordx4 v[64:65], off
	s_mov_b32 m0, s1
	s_cmp_gt_i32 s50, 0
	v_permlane32_swap_b32_e32 v62, v63
	s_cselect_b64 s[46:47], -1, 0
	s_cmp_lt_i32 s50, 1
	v_or_b32_e32 v0, s13, v232
	s_cbranch_scc1 .LBB0_510
	s_waitcnt lgkmcnt(1)
	v_mov_b32_e32 v64, v6
	s_waitcnt lgkmcnt(0)
	v_mov_b32_e32 v65, v2
	v_mov_b32_e32 v2, v7
	v_mov_b32_e32 v6, v8
	v_mov_b32_e32 v7, v4
	v_mov_b32_e32 v4, v9
	v_pk_add_f32 v[2:3], v[64:65], v[2:3]
	v_pk_add_f32 v[4:5], v[6:7], v[4:5]
	v_lshlrev_b32_e32 v45, 16, v50
	v_pk_add_f32 v[2:3], v[2:3], v[4:5]
	v_mul_f32_e32 v66, 0x3d800000, v45
	v_add_f32_e32 v2, v2, v3
	v_mul_f32_e32 v2, 0x39000000, v2
	v_mul_f32_e32 v3, 0x4f800000, v2
	v_cmp_gt_f32_e64 s[0:1], s78, v2
	v_and_b32_e32 v45, 0xffff0000, v50
	v_mul_f32_e32 v67, 0x3d800000, v45
	v_cndmask_b32_e64 v2, v2, v3, s[0:1]
	v_sqrt_f32_e32 v3, v2
	s_mov_b32 s12, 0x40400000
	v_cmp_lt_f32_e64 s[30:31], 0, v66
	v_cmp_lt_f32_e32 vcc, 0, v67
	v_add_u32_e32 v4, -1, v3
	v_fma_f32 v5, -v4, v3, v2
	v_cmp_ge_f32_e64 s[40:41], 0, v5
	v_add_u32_e32 v5, 1, v3
	v_lshlrev_b32_e32 v45, 16, v51
	v_cndmask_b32_e64 v4, v3, v4, s[40:41]
	v_fma_f32 v3, -v5, v3, v2
	v_cmp_lt_f32_e64 s[40:41], 0, v3
	v_mul_f32_e32 v68, 0x3d800000, v45
	v_cmp_lt_f32_e64 s[34:35], 0, v68
	v_cndmask_b32_e64 v3, v4, v5, s[40:41]
	v_add_f32_e32 v5, v56, v57
	v_mul_f32_e32 v6, 0x4f800000, v5
	v_cmp_gt_f32_e64 s[40:41], s78, v5
	v_mul_f32_e32 v4, 0x37800000, v3
	v_cndmask_b32_e64 v3, v3, v4, s[0:1]
	v_cndmask_b32_e64 v5, v5, v6, s[40:41]
	v_sqrt_f32_e32 v6, v5
	v_cmp_class_f32_e64 s[0:1], v2, v231
	v_and_b32_e32 v45, 0xffff0000, v51
	v_mul_f32_e32 v69, 0x3d800000, v45
	v_cndmask_b32_e64 v2, v3, v2, s[0:1]
	v_add_u32_e32 v3, -1, v6
	v_fma_f32 v4, -v3, v6, v5
	v_cmp_ge_f32_e64 s[0:1], 0, v4
	v_add_u32_e32 v4, 1, v6
	v_cmp_lt_f32_e64 s[36:37], 0, v69
	v_cndmask_b32_e64 v3, v6, v3, s[0:1]
	v_fma_f32 v6, -v4, v6, v5
	v_cmp_lt_f32_e64 s[0:1], 0, v6
	v_mov_b32_e32 v55, 0xff800000
	v_mov_b32_e32 v70, 0x7f800000
	v_cndmask_b32_e64 v3, v3, v4, s[0:1]
	v_mul_f32_e32 v4, 0x37800000, v3
	v_cndmask_b32_e64 v3, v3, v4, s[40:41]
	v_cmp_class_f32_e64 s[0:1], v5, v231
	v_add_f32_e32 v4, v58, v59
	v_cndmask_b32_e64 v51, v55, 0, vcc
	v_cndmask_b32_e64 v3, v3, v5, s[0:1]
	v_mul_f32_e32 v5, 0x4f800000, v4
	v_cmp_gt_f32_e64 s[0:1], s78, v4
	v_mul_f32_e64 v3, |v66|, v3
	v_mul_f32_e32 v3, v2, v3
	v_cndmask_b32_e64 v4, v4, v5, s[0:1]
	v_sqrt_f32_e32 v5, v4
	v_fma_f32 v3, v3, s12, 0
	v_cndmask_b32_e64 v6, 0, v3, s[30:31]
	v_cndmask_b32_e64 v3, v3, 0, s[30:31]
	v_add_u32_e32 v7, -1, v5
	v_fma_f32 v8, -v7, v5, v4
	v_cmp_ge_f32_e64 s[40:41], 0, v8
	v_add_u32_e32 v8, 1, v5
	s_mov_b32 s12, 0x467c0400
	v_cndmask_b32_e64 v7, v5, v7, s[40:41]
	v_fma_f32 v5, -v8, v5, v4
	v_cmp_lt_f32_e64 s[40:41], 0, v5
	v_cndmask_b32_e64 v45, v55, 0, s[30:31]
	v_cndmask_b32_e64 v50, 0, v70, s[30:31]
	v_cndmask_b32_e64 v5, v7, v8, s[40:41]
	v_mul_f32_e32 v7, 0x37800000, v5
	v_cndmask_b32_e64 v5, v5, v7, s[0:1]
	v_cmp_class_f32_e64 s[0:1], v4, v231
	v_readlane_b32 s30, v251, 39
	v_cndmask_b32_e64 v53, v55, 0, s[34:35]
	v_cndmask_b32_e64 v4, v5, v4, s[0:1]
	v_add_f32_e32 v5, v60, v61
	v_mul_f32_e32 v7, 0x4f800000, v5
	v_cmp_gt_f32_e64 s[0:1], s78, v5
	v_mul_f32_e64 v4, |v67|, v4
	v_mul_f32_e32 v4, v2, v4
	v_cndmask_b32_e64 v5, v5, v7, s[0:1]
	v_sqrt_f32_e32 v7, v5
	v_fmamk_f32 v8, v4, 0x40400000, v6
	v_cndmask_b32_e32 v6, v6, v8, vcc
	v_fmamk_f32 v4, v4, 0x40400000, v3
	v_add_u32_e32 v8, -1, v7
	v_fma_f32 v9, -v8, v7, v5
	v_cmp_ge_f32_e64 s[40:41], 0, v9
	v_add_u32_e32 v9, 1, v7
	v_cndmask_b32_e32 v3, v4, v3, vcc
	v_cndmask_b32_e64 v8, v7, v8, s[40:41]
	v_fma_f32 v7, -v9, v7, v5
	v_cmp_lt_f32_e64 s[40:41], 0, v7
	v_cndmask_b32_e64 v55, v55, 0, s[36:37]
	v_cndmask_b32_e64 v57, 0, v70, s[34:35]
	v_cndmask_b32_e64 v7, v8, v9, s[40:41]
	v_mul_f32_e32 v8, 0x37800000, v7
	v_cndmask_b32_e64 v7, v7, v8, s[0:1]
	v_cmp_class_f32_e64 s[0:1], v5, v231
	v_cndmask_b32_e64 v58, 0, v70, s[36:37]
	s_mov_b32 s13, 0
	v_cndmask_b32_e64 v5, v7, v5, s[0:1]
	v_add_f32_e32 v7, v62, v63
	v_mul_f32_e32 v8, 0x4f800000, v7
	v_cmp_gt_f32_e64 s[0:1], s78, v7
	v_mul_f32_e64 v5, |v68|, v5
	v_mul_f32_e32 v5, v2, v5
	v_cndmask_b32_e64 v7, v7, v8, s[0:1]
	v_sqrt_f32_e32 v8, v7
	v_fmamk_f32 v9, v5, 0x40400000, v6
	v_cndmask_b32_e64 v6, v6, v9, s[34:35]
	v_fmamk_f32 v4, v5, 0x40400000, v3
	v_add_u32_e32 v9, -1, v8
	v_fma_f32 v56, -v9, v8, v7
	v_cmp_ge_f32_e64 s[40:41], 0, v56
	v_add_u32_e32 v56, 1, v8
	v_cndmask_b32_e64 v3, v4, v3, s[34:35]
	v_cndmask_b32_e64 v9, v8, v9, s[40:41]
	v_fma_f32 v8, -v56, v8, v7
	v_cmp_lt_f32_e64 s[40:41], 0, v8
	s_nop 1
	v_cndmask_b32_e64 v8, v9, v56, s[40:41]
	v_mul_f32_e32 v9, 0x37800000, v8
	v_cndmask_b32_e64 v8, v8, v9, s[0:1]
	v_cmp_class_f32_e64 s[0:1], v7, v231
	v_cndmask_b32_e32 v56, 0, v70, vcc
	s_waitcnt vmcnt(0)
	v_and_b32_e32 v9, 0xffff0000, v41
	v_cndmask_b32_e64 v7, v8, v7, s[0:1]
	v_mul_f32_e64 v7, |v69|, v7
	v_mul_f32_e32 v2, v2, v7
	v_fmamk_f32 v7, v2, 0x40400000, v6
	v_fmamk_f32 v2, v2, 0x40400000, v3
	v_cndmask_b32_e64 v6, v6, v7, s[36:37]
	v_cndmask_b32_e64 v2, v2, v3, s[36:37]
	v_max_f32_e32 v2, v6, v2
	v_div_scale_f32 v3, s[0:1], v2, v2, s12
	v_rcp_f32_e32 v4, v3
	v_and_b32_e32 v8, 0xffff0000, v40
	s_movk_i32 s0, 0x70
	v_readlane_b32 s1, v253, 42
	v_fma_f32 v5, -v3, v4, 1.0
	v_fmac_f32_e32 v4, v5, v4
	v_div_scale_f32 v5, vcc, s12, v2, s12
	v_mul_f32_e32 v6, v5, v4
	v_fma_f32 v7, -v3, v6, v5
	v_fmac_f32_e32 v6, v7, v4
	v_fma_f32 v3, -v3, v6, v5
	v_div_fmas_f32 v3, v3, v4, v6
	v_div_fixup_f32 v3, v3, v2, s12
	v_cmp_lt_f32_e32 vcc, 0, v2
	v_and_b32_e32 v2, 0xffff0000, v38
	v_lshlrev_b32_e32 v5, 16, v39
	v_cndmask_b32_e32 v59, 0, v3, vcc
	v_mul_f32_e32 v6, v69, v59
	v_and_b32_e32 v3, 0xffff0000, v39
	v_pk_mul_f32 v[2:3], v[6:7], v[2:3] op_sel_hi:[0,1]
	v_lshlrev_b32_e32 v4, 16, v38
	v_pk_mul_f32 v[8:9], v[6:7], v[8:9] op_sel_hi:[0,1]
	v_lshlrev_b32_e32 v39, 16, v41
	v_lshlrev_b32_e32 v38, 16, v40
	v_pk_mul_f32 v[4:5], v[6:7], v[4:5] op_sel_hi:[0,1]
	v_pk_mul_f32 v[38:39], v[6:7], v[38:39] op_sel_hi:[0,1]
	v_bfe_u32 v7, v9, 16, 1
	v_bfe_u32 v41, v3, 16, 1
	v_bfe_u32 v40, v8, 16, 1
	v_bfe_u32 v60, v2, 16, 1
	v_add3_u32 v3, v3, v41, s39
	v_add3_u32 v7, v9, v7, s39
	v_bfe_u32 v9, v4, 16, 1
	v_bfe_u32 v41, v38, 16, 1
	v_add3_u32 v2, v2, v60, s39
	v_add3_u32 v8, v8, v40, s39
	v_bfe_u32 v40, v5, 16, 1
	v_bfe_u32 v60, v39, 16, 1
	v_add3_u32 v38, v38, v41, s39
	v_add3_u32 v4, v4, v9, s39
	v_add3_u32 v39, v39, v60, s39
	v_add3_u32 v5, v5, v40, s39
	v_lshrrev_b32_e32 v9, 16, v4
	v_lshrrev_b32_e32 v4, 16, v38
	v_lshrrev_b32_e32 v40, 16, v5
	v_lshrrev_b32_e32 v5, 16, v39
	v_and_or_b32 v4, v8, s38, v4
	v_and_or_b32 v2, v2, s38, v9
	v_and_b32_e32 v9, 0xffff0000, v35
	v_and_b32_e32 v8, 0xffff0000, v34
	v_and_b32_e32 v39, 0xffff0000, v37
	v_and_b32_e32 v38, 0xffff0000, v36
	v_pk_mul_f32 v[8:9], v[6:7], v[8:9] op_sel_hi:[0,1]
	v_lshlrev_b32_e32 v35, 16, v35
	v_lshlrev_b32_e32 v34, 16, v34
	v_pk_mul_f32 v[38:39], v[6:7], v[38:39] op_sel_hi:[0,1]
	v_lshlrev_b32_e32 v37, 16, v37
	v_lshlrev_b32_e32 v36, 16, v36
	v_and_or_b32 v5, v7, s38, v5
	v_and_or_b32 v3, v3, s38, v40
	v_pk_mul_f32 v[34:35], v[6:7], v[34:35] op_sel_hi:[0,1]
	v_pk_mul_f32 v[6:7], v[6:7], v[36:37] op_sel_hi:[0,1]
	v_bfe_u32 v36, v39, 16, 1
	v_bfe_u32 v37, v38, 16, 1
	v_bfe_u32 v40, v9, 16, 1
	v_bfe_u32 v41, v8, 16, 1
	v_add3_u32 v41, v8, v41, s39
	v_add3_u32 v40, v9, v40, s39
	v_add3_u32 v8, v38, v37, s39
	v_add3_u32 v9, v39, v36, s39
	v_bfe_u32 v36, v34, 16, 1
	v_bfe_u32 v38, v6, 16, 1
	v_bfe_u32 v37, v35, 16, 1
	v_add3_u32 v6, v6, v38, s39
	v_add3_u32 v34, v34, v36, s39
	v_bfe_u32 v39, v7, 16, 1
	v_add3_u32 v35, v35, v37, s39
	v_lshrrev_b32_e32 v34, 16, v34
	v_lshrrev_b32_e32 v6, 16, v6
	v_add3_u32 v7, v7, v39, s39
	v_lshrrev_b32_e32 v35, 16, v35
	v_and_or_b32 v8, v8, s38, v6
	v_and_or_b32 v6, v41, s38, v34
	v_mul_f32_e32 v34, v68, v59
	v_and_b32_e32 v37, 0xffff0000, v11
	v_and_b32_e32 v36, 0xffff0000, v10
	v_and_b32_e32 v39, 0xffff0000, v13
	v_and_b32_e32 v38, 0xffff0000, v12
	v_lshrrev_b32_e32 v7, 16, v7
	v_pk_mul_f32 v[36:37], v[34:35], v[36:37] op_sel_hi:[0,1]
	v_lshlrev_b32_e32 v11, 16, v11
	v_lshlrev_b32_e32 v10, 16, v10
	v_pk_mul_f32 v[38:39], v[34:35], v[38:39] op_sel_hi:[0,1]
	v_lshlrev_b32_e32 v13, 16, v13
	v_lshlrev_b32_e32 v12, 16, v12
	v_and_or_b32 v9, v9, s38, v7
	v_and_or_b32 v7, v40, s38, v35
	v_pk_mul_f32 v[10:11], v[34:35], v[10:11] op_sel_hi:[0,1]
	v_pk_mul_f32 v[12:13], v[34:35], v[12:13] op_sel_hi:[0,1]
	v_bfe_u32 v35, v39, 16, 1
	v_bfe_u32 v40, v38, 16, 1
	v_bfe_u32 v41, v37, 16, 1
	v_add3_u32 v37, v37, v41, s39
	v_add3_u32 v38, v38, v40, s39
	v_add3_u32 v35, v39, v35, s39
	v_bfe_u32 v39, v10, 16, 1
	v_bfe_u32 v40, v11, 16, 1
	v_bfe_u32 v41, v12, 16, 1
	v_bfe_u32 v60, v36, 16, 1
	v_add3_u32 v12, v12, v41, s39
	v_add3_u32 v11, v11, v40, s39
	v_add3_u32 v10, v10, v39, s39
	v_add3_u32 v36, v36, v60, s39
	v_bfe_u32 v60, v13, 16, 1
	v_lshrrev_b32_e32 v10, 16, v10
	v_lshrrev_b32_e32 v11, 16, v11
	v_lshrrev_b32_e32 v12, 16, v12
	v_add3_u32 v13, v13, v60, s39
	v_and_or_b32 v12, v38, s38, v12
	v_and_or_b32 v11, v37, s38, v11
	v_and_or_b32 v10, v36, s38, v10
	v_and_b32_e32 v37, 0xffff0000, v15
	v_and_b32_e32 v36, 0xffff0000, v14
	v_and_b32_e32 v39, 0xffff0000, v17
	v_and_b32_e32 v38, 0xffff0000, v16
	v_lshrrev_b32_e32 v13, 16, v13
	v_pk_mul_f32 v[36:37], v[34:35], v[36:37] op_sel_hi:[0,1]
	v_lshlrev_b32_e32 v15, 16, v15
	v_lshlrev_b32_e32 v14, 16, v14
	v_pk_mul_f32 v[38:39], v[34:35], v[38:39] op_sel_hi:[0,1]
	v_lshlrev_b32_e32 v17, 16, v17
	v_lshlrev_b32_e32 v16, 16, v16
	v_and_or_b32 v13, v35, s38, v13
	v_pk_mul_f32 v[14:15], v[34:35], v[14:15] op_sel_hi:[0,1]
	v_pk_mul_f32 v[16:17], v[34:35], v[16:17] op_sel_hi:[0,1]
	v_bfe_u32 v34, v39, 16, 1
	v_bfe_u32 v35, v38, 16, 1
	v_bfe_u32 v41, v36, 16, 1
	v_add3_u32 v36, v36, v41, s39
	v_add3_u32 v35, v38, v35, s39
	v_add3_u32 v34, v39, v34, s39
	v_bfe_u32 v38, v14, 16, 1
	v_bfe_u32 v39, v15, 16, 1
	v_bfe_u32 v41, v17, 16, 1
	v_bfe_u32 v40, v37, 16, 1
	v_add3_u32 v17, v17, v41, s39
	v_add3_u32 v15, v15, v39, s39
	v_add3_u32 v14, v14, v38, s39
	v_add3_u32 v37, v37, v40, s39
	v_bfe_u32 v40, v16, 16, 1
	v_lshrrev_b32_e32 v14, 16, v14
	v_lshrrev_b32_e32 v15, 16, v15
	v_lshrrev_b32_e32 v17, 16, v17
	v_add3_u32 v16, v16, v40, s39
	v_and_or_b32 v17, v34, s38, v17
	v_and_or_b32 v15, v37, s38, v15
	v_and_or_b32 v14, v36, s38, v14
	v_mul_f32_e32 v34, v67, v59
	v_and_b32_e32 v37, 0xffff0000, v19
	v_and_b32_e32 v36, 0xffff0000, v18
	v_and_b32_e32 v39, 0xffff0000, v21
	v_and_b32_e32 v38, 0xffff0000, v20
	v_lshrrev_b32_e32 v16, 16, v16
	v_pk_mul_f32 v[36:37], v[34:35], v[36:37] op_sel_hi:[0,1]
	v_lshlrev_b32_e32 v19, 16, v19
	v_lshlrev_b32_e32 v18, 16, v18
	v_pk_mul_f32 v[38:39], v[34:35], v[38:39] op_sel_hi:[0,1]
	v_lshlrev_b32_e32 v21, 16, v21
	v_lshlrev_b32_e32 v20, 16, v20
	v_and_or_b32 v16, v35, s38, v16
	v_pk_mul_f32 v[18:19], v[34:35], v[18:19] op_sel_hi:[0,1]
	v_pk_mul_f32 v[20:21], v[34:35], v[20:21] op_sel_hi:[0,1]
	v_bfe_u32 v35, v39, 16, 1
	v_bfe_u32 v40, v38, 16, 1
	v_bfe_u32 v41, v37, 16, 1
	v_add3_u32 v37, v37, v41, s39
	v_add3_u32 v38, v38, v40, s39
	v_add3_u32 v35, v39, v35, s39
	v_bfe_u32 v39, v18, 16, 1
	v_bfe_u32 v40, v19, 16, 1
	v_bfe_u32 v41, v20, 16, 1
	v_bfe_u32 v60, v36, 16, 1
	v_add3_u32 v20, v20, v41, s39
	v_add3_u32 v19, v19, v40, s39
	v_add3_u32 v18, v18, v39, s39
	v_add3_u32 v36, v36, v60, s39
	v_bfe_u32 v60, v21, 16, 1
	v_lshrrev_b32_e32 v18, 16, v18
	v_lshrrev_b32_e32 v19, 16, v19
	v_lshrrev_b32_e32 v20, 16, v20
	v_add3_u32 v21, v21, v60, s39
	v_and_or_b32 v20, v38, s38, v20
	v_and_or_b32 v19, v37, s38, v19
	v_and_or_b32 v18, v36, s38, v18
	v_and_b32_e32 v37, 0xffff0000, v23
	v_and_b32_e32 v36, 0xffff0000, v22
	v_and_b32_e32 v39, 0xffff0000, v25
	v_and_b32_e32 v38, 0xffff0000, v24
	v_lshrrev_b32_e32 v21, 16, v21
	v_pk_mul_f32 v[36:37], v[34:35], v[36:37] op_sel_hi:[0,1]
	v_lshlrev_b32_e32 v23, 16, v23
	v_lshlrev_b32_e32 v22, 16, v22
	v_pk_mul_f32 v[38:39], v[34:35], v[38:39] op_sel_hi:[0,1]
	v_lshlrev_b32_e32 v25, 16, v25
	v_lshlrev_b32_e32 v24, 16, v24
	v_and_or_b32 v21, v35, s38, v21
	v_pk_mul_f32 v[22:23], v[34:35], v[22:23] op_sel_hi:[0,1]
	v_pk_mul_f32 v[24:25], v[34:35], v[24:25] op_sel_hi:[0,1]
	v_bfe_u32 v34, v39, 16, 1
	v_bfe_u32 v35, v38, 16, 1
	v_bfe_u32 v41, v36, 16, 1
	v_add3_u32 v36, v36, v41, s39
	v_add3_u32 v35, v38, v35, s39
	v_add3_u32 v34, v39, v34, s39
	v_bfe_u32 v38, v22, 16, 1
	v_bfe_u32 v39, v23, 16, 1
	v_bfe_u32 v41, v25, 16, 1
	v_bfe_u32 v40, v37, 16, 1
	v_add3_u32 v25, v25, v41, s39
	v_add3_u32 v23, v23, v39, s39
	v_add3_u32 v22, v22, v38, s39
	v_add3_u32 v37, v37, v40, s39
	v_lshrrev_b32_e32 v22, 16, v22
	v_lshrrev_b32_e32 v23, 16, v23
	v_lshrrev_b32_e32 v25, 16, v25
	v_bfe_u32 v40, v24, 16, 1
	v_and_or_b32 v25, v34, s38, v25
	v_and_or_b32 v23, v37, s38, v23
	v_and_or_b32 v22, v36, s38, v22
	v_mul_f32_e32 v34, v66, v59
	v_and_b32_e32 v37, 0xffff0000, v27
	v_and_b32_e32 v36, 0xffff0000, v26
	v_add3_u32 v24, v24, v40, s39
	v_pk_mul_f32 v[36:37], v[34:35], v[36:37] op_sel_hi:[0,1]
	v_and_b32_e32 v39, 0xffff0000, v29
	v_and_b32_e32 v38, 0xffff0000, v28
	v_lshlrev_b32_e32 v29, 16, v29
	v_lshlrev_b32_e32 v28, 16, v28
	v_lshrrev_b32_e32 v24, 16, v24
	v_lshlrev_b32_e32 v27, 16, v27
	v_lshlrev_b32_e32 v26, 16, v26
	v_pk_mul_f32 v[38:39], v[34:35], v[38:39] op_sel_hi:[0,1]
	v_pk_mul_f32 v[28:29], v[34:35], v[28:29] op_sel_hi:[0,1]
	v_bfe_u32 v41, v37, 16, 1
	v_and_or_b32 v24, v35, s38, v24
	v_pk_mul_f32 v[26:27], v[34:35], v[26:27] op_sel_hi:[0,1]
	v_bfe_u32 v35, v39, 16, 1
	v_bfe_u32 v40, v38, 16, 1
	v_add3_u32 v37, v37, v41, s39
	v_bfe_u32 v41, v28, 16, 1
	v_bfe_u32 v59, v36, 16, 1
	v_add3_u32 v38, v38, v40, s39
	v_add3_u32 v35, v39, v35, s39
	v_bfe_u32 v39, v26, 16, 1
	v_bfe_u32 v40, v27, 16, 1
	v_add3_u32 v28, v28, v41, s39
	v_add3_u32 v36, v36, v59, s39
	v_bfe_u32 v59, v29, 16, 1
	v_add3_u32 v27, v27, v40, s39
	v_add3_u32 v26, v26, v39, s39
	v_lshrrev_b32_e32 v28, 16, v28
	v_add3_u32 v29, v29, v59, s39
	v_lshrrev_b32_e32 v26, 16, v26
	v_lshrrev_b32_e32 v27, 16, v27
	v_and_or_b32 v28, v38, s38, v28
	v_and_b32_e32 v39, 0xffff0000, v33
	v_and_b32_e32 v38, 0xffff0000, v32
	v_lshrrev_b32_e32 v29, 16, v29
	v_and_or_b32 v27, v37, s38, v27
	v_and_or_b32 v26, v36, s38, v26
	v_and_b32_e32 v37, 0xffff0000, v31
	v_and_b32_e32 v36, 0xffff0000, v30
	v_lshlrev_b32_e32 v31, 16, v31
	v_lshlrev_b32_e32 v30, 16, v30
	v_pk_mul_f32 v[38:39], v[34:35], v[38:39] op_sel_hi:[0,1]
	v_lshlrev_b32_e32 v33, 16, v33
	v_lshlrev_b32_e32 v32, 16, v32
	v_and_or_b32 v29, v35, s38, v29
	v_pk_mul_f32 v[36:37], v[34:35], v[36:37] op_sel_hi:[0,1]
	v_pk_mul_f32 v[30:31], v[34:35], v[30:31] op_sel_hi:[0,1]
	v_pk_mul_f32 v[32:33], v[34:35], v[32:33] op_sel_hi:[0,1]
	v_bfe_u32 v34, v39, 16, 1
	v_bfe_u32 v35, v38, 16, 1
	v_add3_u32 v35, v38, v35, s39
	v_add3_u32 v34, v39, v34, s39
	v_bfe_u32 v38, v30, 16, 1
	v_bfe_u32 v39, v31, 16, 1
	v_add3_u32 v31, v31, v39, s39
	v_add3_u32 v30, v30, v38, s39
	v_and_b32_e32 v38, -16, v42
	v_lshlrev_b32_e32 v39, 4, v232
	v_bfe_u32 v41, v36, 16, 1
	s_add_i32 s12, s50, -1
	v_bitop3_b32 v61, v39, v38, s0 bitop3:0x6c
	v_add_u32_e32 v38, 64, v38
	v_add3_u32 v36, v36, v41, s39
	v_bfe_u32 v41, v33, 16, 1
	v_bitop3_b32 v38, v39, v38, s0 bitop3:0x6c
	s_lshl_b32 s0, s12, 5
	v_add3_u32 v33, v33, v41, s39
	v_lshlrev_b32_e32 v59, 7, v232
	v_ashrrev_i32_e32 v41, 2, v42
	s_add_i32 s0, s0, s30
	v_bfe_u32 v40, v37, 16, 1
	v_and_b32_e32 v60, -4, v41
	v_add3_u32 v41, v38, v59, s1
	v_add3_u32 v59, v61, v59, s1
	s_ashr_i32 s1, s0, 31
	v_add3_u32 v37, v37, v40, s39
	v_bfe_u32 v40, v32, 16, 1
	s_lshl_b64 s[0:1], s[0:1], 9
	v_add3_u32 v32, v32, v40, s39
	v_lshrrev_b32_e32 v30, 16, v30
	v_lshrrev_b32_e32 v31, 16, v31
	s_add_u32 s0, s4, s0
	v_lshrrev_b32_e32 v32, 16, v32
	v_lshrrev_b32_e32 v33, 16, v33
	v_and_or_b32 v31, v37, s38, v31
	v_and_or_b32 v30, v36, s38, v30
	v_lshlrev_b64 v[36:37], 3, v[42:43]
	s_addc_u32 s1, s5, s1
	v_and_or_b32 v33, v34, s38, v33
	v_and_or_b32 v32, v35, s38, v32
	v_lshl_add_u64 v[34:35], s[4:5], 0, v[36:37]
	v_lshl_add_u64 v[36:37], s[0:1], 0, v[36:37]
	s_lshl_b32 s0, s50, 7
	v_readlane_b32 s1, v254, 10
	s_add_i32 s0, s1, s0
	s_mov_b32 s100, 0
	v_lshl_add_u32 v40, v0, 10, 0
	v_add_u32_e32 v60, s0, v60
	s_mov_b32 s0, 0
	s_waitcnt vmcnt(0)
	s_branch .LBB0_500

.LBB0_502:
	s_and_b32 s1, s13, 0x4000
	v_add_u32_e32 v61, s1, v41
	v_add_u32_e32 v62, s1, v59
	s_cmp_eq_u32 s0, s12
	s_mov_b64 s[0:1], -1
	s_cbranch_scc1 .LBB0_506
	s_mov_b32 s0, s30
	s_ashr_i32 s1, s0, 31
	s_lshl_b64 s[34:35], s[0:1], 9
	ds_read_b128 v[72:75], v62
	ds_read_b128 v[76:79], v61
	ds_read_b128 v[80:83], v62 offset:4096
	ds_read_b128 v[84:87], v61 offset:4096
	ds_read_b128 v[88:91], v62 offset:8192
	ds_read_b128 v[92:95], v61 offset:8192
	ds_read_b128 v[96:99], v62 offset:12288
	ds_read_b128 v[100:103], v61 offset:12288
	v_lshl_add_u64 v[168:169], v[34:35], 0, s[34:35]
	s_cmp_eq_u32 s100, 0
	s_cbranch_scc1 .Lp1_first_a
	v_med3_f32 v170, v136, v45, v50
	v_med3_f32 v178, v140, v51, v56
	v_med3_f32 v171, v144, v53, v57
	v_med3_f32 v179, v148, v55, v58
	v_med3_f32 v172, v137, v45, v50
	v_med3_f32 v180, v141, v51, v56
	v_med3_f32 v173, v145, v53, v57
	v_med3_f32 v181, v149, v55, v58
	v_med3_f32 v174, v138, v45, v50
	v_med3_f32 v182, v142, v51, v56
	v_med3_f32 v175, v146, v53, v57
	v_med3_f32 v183, v150, v55, v58
	v_med3_f32 v176, v139, v45, v50
	v_med3_f32 v184, v143, v51, v56
	v_med3_f32 v177, v147, v53, v57
	v_med3_f32 v185, v151, v55, v58
	s_waitcnt lgkmcnt(0)
	v_pk_add_f32 v[170:171], v[170:171], v[178:179]
	v_pk_add_f32 v[172:173], v[172:173], v[180:181]
	v_pk_add_f32 v[174:175], v[174:175], v[182:183]
	v_pk_add_f32 v[176:177], v[176:177], v[184:185]
	v_add_f32_e32 v186, v170, v171
	v_add_f32_e32 v187, v172, v173
	v_mfma_f32_16x16x32_bf16 v[104:107], v[72:75], v[30:33], 0
	v_add_f32_e32 v188, v174, v175
	v_add_f32_e32 v189, v176, v177
	v_cvt_pkrtz_f16_f32 v190, v186, v187
	v_cvt_pkrtz_f16_f32 v191, v188, v189
	global_store_dwordx2 v[208:209], v[190:191], off offset:1024
	v_cvt_f32_f16_e32 v192, v190
	v_mfma_f32_16x16x32_bf16 v[108:111], v[72:75], v[22:25], 0
	v_cvt_f32_f16_sdwa v193, v190 dst_sel:DWORD dst_unused:UNUSED_PAD src0_sel:WORD_1
	v_cvt_f32_f16_e32 v194, v191
	v_cvt_f32_f16_sdwa v195, v191 dst_sel:DWORD dst_unused:UNUSED_PAD src0_sel:WORD_1
	v_sqrt_f32_e64 v170, |v192|
	v_sqrt_f32_e64 v171, |v193|
	v_sqrt_f32_e64 v172, |v194|
	v_mfma_f32_16x16x32_bf16 v[112:115], v[72:75], v[14:17], 0
	v_sqrt_f32_e64 v173, |v195|
	v_ceil_f32_e32 v170, v170
	v_ceil_f32_e32 v171, v171
	v_ceil_f32_e32 v172, v172
	v_ceil_f32_e32 v173, v173
	v_min_f32_e32 v170, 0x42fe0000, v170
	v_mfma_f32_16x16x32_bf16 v[116:119], v[72:75], v[6:9], 0
	v_min_f32_e32 v171, 0x42fe0000, v171
	v_min_f32_e32 v172, 0x42fe0000, v172
	v_min_f32_e32 v173, 0x42fe0000, v173
	v_bfi_b32 v170, s10, v170, v192
	v_bfi_b32 v171, s10, v171, v193
	v_bfi_b32 v172, s10, v172, v194
	v_mfma_f32_16x16x32_bf16 v[104:107], v[76:79], v[26:29], v[104:107]
	v_bfi_b32 v173, s10, v173, v195
	v_cvt_i32_f32_e32 v170, v170
	v_cvt_i32_f32_e32 v171, v171
	v_cvt_i32_f32_e32 v172, v172
	v_cvt_i32_f32_e32 v173, v173
	v_lshl_add_u32 v170, v170, 2, v40
	v_mfma_f32_16x16x32_bf16 v[108:111], v[76:79], v[18:21], v[108:111]
	v_lshl_add_u32 v171, v171, 2, v40
	v_lshl_add_u32 v172, v172, 2, v40
	v_lshl_add_u32 v173, v173, 2, v40
	ds_add_u32 v170, v245 offset:33280
	ds_add_u32 v171, v245 offset:33280
	ds_add_u32 v172, v245 offset:33280
	v_mfma_f32_16x16x32_bf16 v[112:115], v[76:79], v[10:13], v[112:115]
	ds_add_u32 v173, v245 offset:33280
	v_med3_f32 v170, v152, v45, v50
	v_med3_f32 v178, v156, v51, v56
	v_med3_f32 v171, v160, v53, v57
	v_med3_f32 v179, v164, v55, v58
	v_med3_f32 v172, v153, v45, v50
	v_mfma_f32_16x16x32_bf16 v[116:119], v[76:79], v[2:5], v[116:119]
	v_med3_f32 v180, v157, v51, v56
	v_med3_f32 v173, v161, v53, v57
	v_med3_f32 v181, v165, v55, v58
	v_med3_f32 v174, v154, v45, v50
	v_med3_f32 v182, v158, v51, v56
	v_med3_f32 v175, v162, v53, v57
	v_mfma_f32_16x16x32_bf16 v[120:123], v[80:83], v[30:33], 0
	v_med3_f32 v183, v166, v55, v58
	v_med3_f32 v176, v155, v45, v50
	v_med3_f32 v184, v159, v51, v56
	v_med3_f32 v177, v163, v53, v57
	v_med3_f32 v185, v167, v55, v58
	v_pk_add_f32 v[170:171], v[170:171], v[178:179]
	v_mfma_f32_16x16x32_bf16 v[124:127], v[80:83], v[22:25], 0
	v_pk_add_f32 v[172:173], v[172:173], v[180:181]
	v_pk_add_f32 v[174:175], v[174:175], v[182:183]
	v_pk_add_f32 v[176:177], v[176:177], v[184:185]
	v_add_f32_e32 v186, v170, v171
	v_add_f32_e32 v187, v172, v173
	v_add_f32_e32 v188, v174, v175
	v_mfma_f32_16x16x32_bf16 v[128:131], v[80:83], v[14:17], 0
	v_add_f32_e32 v189, v176, v177
	v_cvt_pkrtz_f16_f32 v190, v186, v187
	v_cvt_pkrtz_f16_f32 v191, v188, v189
	global_store_dwordx2 v[208:209], v[190:191], off offset:1536
	v_cvt_f32_f16_e32 v192, v190
	v_cvt_f32_f16_sdwa v193, v190 dst_sel:DWORD dst_unused:UNUSED_PAD src0_sel:WORD_1
	v_mfma_f32_16x16x32_bf16 v[132:135], v[80:83], v[6:9], 0
	v_cvt_f32_f16_e32 v194, v191
	v_cvt_f32_f16_sdwa v195, v191 dst_sel:DWORD dst_unused:UNUSED_PAD src0_sel:WORD_1
	v_sqrt_f32_e64 v170, |v192|
	v_sqrt_f32_e64 v171, |v193|
	v_sqrt_f32_e64 v172, |v194|
	v_sqrt_f32_e64 v173, |v195|
	v_mfma_f32_16x16x32_bf16 v[120:123], v[84:87], v[26:29], v[120:123]
	v_ceil_f32_e32 v170, v170
	v_ceil_f32_e32 v171, v171
	v_ceil_f32_e32 v172, v172
	v_ceil_f32_e32 v173, v173
	v_min_f32_e32 v170, 0x42fe0000, v170
	v_min_f32_e32 v171, 0x42fe0000, v171
	v_mfma_f32_16x16x32_bf16 v[124:127], v[84:87], v[18:21], v[124:127]
	v_min_f32_e32 v172, 0x42fe0000, v172
	v_min_f32_e32 v173, 0x42fe0000, v173
	v_bfi_b32 v170, s10, v170, v192
	v_bfi_b32 v171, s10, v171, v193
	v_bfi_b32 v172, s10, v172, v194
	v_bfi_b32 v173, s10, v173, v195
	v_mfma_f32_16x16x32_bf16 v[128:131], v[84:87], v[10:13], v[128:131]
	v_cvt_i32_f32_e32 v170, v170
	v_cvt_i32_f32_e32 v171, v171
	v_cvt_i32_f32_e32 v172, v172
	v_cvt_i32_f32_e32 v173, v173
	v_lshl_add_u32 v170, v170, 2, v40
	v_lshl_add_u32 v171, v171, 2, v40
	v_mfma_f32_16x16x32_bf16 v[132:135], v[84:87], v[2:5], v[132:135]
	v_lshl_add_u32 v172, v172, 2, v40
	v_lshl_add_u32 v173, v173, 2, v40
	ds_add_u32 v170, v245 offset:33280
	ds_add_u32 v171, v245 offset:33280
	ds_add_u32 v172, v245 offset:33280
	ds_add_u32 v173, v245 offset:33280
	s_branch .Lp1_common_a
.Lp1_first_a:
	s_waitcnt lgkmcnt(7)
	v_mfma_f32_16x16x32_bf16 v[104:107], v[72:75], v[30:33], 0
	v_mfma_f32_16x16x32_bf16 v[108:111], v[72:75], v[22:25], 0
	v_mfma_f32_16x16x32_bf16 v[112:115], v[72:75], v[14:17], 0
	v_mfma_f32_16x16x32_bf16 v[116:119], v[72:75], v[6:9], 0
	s_waitcnt lgkmcnt(6)
	v_mfma_f32_16x16x32_bf16 v[104:107], v[76:79], v[26:29], v[104:107]
	v_mfma_f32_16x16x32_bf16 v[108:111], v[76:79], v[18:21], v[108:111]
	v_mfma_f32_16x16x32_bf16 v[112:115], v[76:79], v[10:13], v[112:115]
	v_mfma_f32_16x16x32_bf16 v[116:119], v[76:79], v[2:5], v[116:119]
	s_waitcnt lgkmcnt(5)
	v_mfma_f32_16x16x32_bf16 v[120:123], v[80:83], v[30:33], 0
	v_mfma_f32_16x16x32_bf16 v[124:127], v[80:83], v[22:25], 0
	v_mfma_f32_16x16x32_bf16 v[128:131], v[80:83], v[14:17], 0
	v_mfma_f32_16x16x32_bf16 v[132:135], v[80:83], v[6:9], 0
	s_waitcnt lgkmcnt(4)
	v_mfma_f32_16x16x32_bf16 v[120:123], v[84:87], v[26:29], v[120:123]
	v_mfma_f32_16x16x32_bf16 v[124:127], v[84:87], v[18:21], v[124:127]
	v_mfma_f32_16x16x32_bf16 v[128:131], v[84:87], v[10:13], v[128:131]
	v_mfma_f32_16x16x32_bf16 v[132:135], v[84:87], v[2:5], v[132:135]
	s_waitcnt lgkmcnt(0)
.Lp1_common_a:
	v_mov_b64_e32 v[208:209], v[168:169]
	v_med3_f32 v170, v104, v45, v50
	v_med3_f32 v178, v108, v51, v56
	v_med3_f32 v171, v112, v53, v57
	v_med3_f32 v179, v116, v55, v58
	v_med3_f32 v172, v105, v45, v50
	v_med3_f32 v180, v109, v51, v56
	v_mfma_f32_16x16x32_bf16 v[136:139], v[88:91], v[30:33], 0
	v_med3_f32 v173, v113, v53, v57
	v_med3_f32 v181, v117, v55, v58
	v_med3_f32 v174, v106, v45, v50
	v_med3_f32 v182, v110, v51, v56
	v_med3_f32 v175, v114, v53, v57
	v_med3_f32 v183, v118, v55, v58
	v_mfma_f32_16x16x32_bf16 v[140:143], v[88:91], v[22:25], 0
	v_med3_f32 v176, v107, v45, v50
	v_med3_f32 v184, v111, v51, v56
	v_med3_f32 v177, v115, v53, v57
	v_med3_f32 v185, v119, v55, v58
	v_pk_add_f32 v[170:171], v[170:171], v[178:179]
	v_pk_add_f32 v[172:173], v[172:173], v[180:181]
	v_mfma_f32_16x16x32_bf16 v[144:147], v[88:91], v[14:17], 0
	v_pk_add_f32 v[174:175], v[174:175], v[182:183]
	v_pk_add_f32 v[176:177], v[176:177], v[184:185]
	v_add_f32_e32 v186, v170, v171
	v_add_f32_e32 v187, v172, v173
	v_add_f32_e32 v188, v174, v175
	v_add_f32_e32 v189, v176, v177
	v_mfma_f32_16x16x32_bf16 v[148:151], v[88:91], v[6:9], 0
	v_cvt_pkrtz_f16_f32 v190, v186, v187
	v_cvt_pkrtz_f16_f32 v191, v188, v189
	global_store_dwordx2 v[168:169], v[190:191], off
	v_cvt_f32_f16_e32 v192, v190
	v_cvt_f32_f16_sdwa v193, v190 dst_sel:DWORD dst_unused:UNUSED_PAD src0_sel:WORD_1
	v_cvt_f32_f16_e32 v194, v191
	v_mfma_f32_16x16x32_bf16 v[136:139], v[92:95], v[26:29], v[136:139]
	v_cvt_f32_f16_sdwa v195, v191 dst_sel:DWORD dst_unused:UNUSED_PAD src0_sel:WORD_1
	v_sqrt_f32_e64 v170, |v192|
	v_sqrt_f32_e64 v171, |v193|
	v_sqrt_f32_e64 v172, |v194|
	v_sqrt_f32_e64 v173, |v195|
	v_ceil_f32_e32 v170, v170
	v_mfma_f32_16x16x32_bf16 v[140:143], v[92:95], v[18:21], v[140:143]
	v_ceil_f32_e32 v171, v171
	v_ceil_f32_e32 v172, v172
	v_ceil_f32_e32 v173, v173
	v_min_f32_e32 v170, 0x42fe0000, v170
	v_min_f32_e32 v171, 0x42fe0000, v171
	v_min_f32_e32 v172, 0x42fe0000, v172
	v_mfma_f32_16x16x32_bf16 v[144:147], v[92:95], v[10:13], v[144:147]
	v_min_f32_e32 v173, 0x42fe0000, v173
	v_bfi_b32 v170, s10, v170, v192
	v_bfi_b32 v171, s10, v171, v193
	v_bfi_b32 v172, s10, v172, v194
	v_bfi_b32 v173, s10, v173, v195
	v_cvt_i32_f32_e32 v170, v170
	v_mfma_f32_16x16x32_bf16 v[148:151], v[92:95], v[2:5], v[148:151]
	v_cvt_i32_f32_e32 v171, v171
	v_cvt_i32_f32_e32 v172, v172
	v_cvt_i32_f32_e32 v173, v173
	v_lshl_add_u32 v170, v170, 2, v40
	v_lshl_add_u32 v171, v171, 2, v40
	v_lshl_add_u32 v172, v172, 2, v40
	v_lshl_add_u32 v173, v173, 2, v40
	ds_add_u32 v170, v245 offset:33280
	ds_add_u32 v171, v245 offset:33280
	ds_add_u32 v172, v245 offset:33280
	ds_add_u32 v173, v245 offset:33280
	v_med3_f32 v170, v120, v45, v50
	v_med3_f32 v178, v124, v51, v56
	v_med3_f32 v171, v128, v53, v57
	v_med3_f32 v179, v132, v55, v58
	v_med3_f32 v172, v121, v45, v50
	v_med3_f32 v180, v125, v51, v56
	v_mfma_f32_16x16x32_bf16 v[152:155], v[96:99], v[30:33], 0
	v_med3_f32 v173, v129, v53, v57
	v_med3_f32 v181, v133, v55, v58
	v_med3_f32 v174, v122, v45, v50
	v_med3_f32 v182, v126, v51, v56
	v_med3_f32 v175, v130, v53, v57
	v_med3_f32 v183, v134, v55, v58
	v_mfma_f32_16x16x32_bf16 v[156:159], v[96:99], v[22:25], 0
	v_med3_f32 v176, v123, v45, v50
	v_med3_f32 v184, v127, v51, v56
	v_med3_f32 v177, v131, v53, v57
	v_med3_f32 v185, v135, v55, v58
	v_pk_add_f32 v[170:171], v[170:171], v[178:179]
	v_pk_add_f32 v[172:173], v[172:173], v[180:181]
	v_mfma_f32_16x16x32_bf16 v[160:163], v[96:99], v[14:17], 0
	v_pk_add_f32 v[174:175], v[174:175], v[182:183]
	v_pk_add_f32 v[176:177], v[176:177], v[184:185]
	v_add_f32_e32 v186, v170, v171
	v_add_f32_e32 v187, v172, v173
	v_add_f32_e32 v188, v174, v175
	v_add_f32_e32 v189, v176, v177
	v_mfma_f32_16x16x32_bf16 v[164:167], v[96:99], v[6:9], 0
	v_cvt_pkrtz_f16_f32 v190, v186, v187
	v_cvt_pkrtz_f16_f32 v191, v188, v189
	global_store_dwordx2 v[168:169], v[190:191], off offset:512
	v_cvt_f32_f16_e32 v192, v190
	v_cvt_f32_f16_sdwa v193, v190 dst_sel:DWORD dst_unused:UNUSED_PAD src0_sel:WORD_1
	v_cvt_f32_f16_e32 v194, v191
	v_mfma_f32_16x16x32_bf16 v[152:155], v[100:103], v[26:29], v[152:155]
	v_cvt_f32_f16_sdwa v195, v191 dst_sel:DWORD dst_unused:UNUSED_PAD src0_sel:WORD_1
	v_sqrt_f32_e64 v170, |v192|
	v_sqrt_f32_e64 v171, |v193|
	v_sqrt_f32_e64 v172, |v194|
	v_sqrt_f32_e64 v173, |v195|
	v_ceil_f32_e32 v170, v170
	v_mfma_f32_16x16x32_bf16 v[156:159], v[100:103], v[18:21], v[156:159]
	v_ceil_f32_e32 v171, v171
	v_ceil_f32_e32 v172, v172
	v_ceil_f32_e32 v173, v173
	v_min_f32_e32 v170, 0x42fe0000, v170
	v_min_f32_e32 v171, 0x42fe0000, v171
	v_min_f32_e32 v172, 0x42fe0000, v172
	v_mfma_f32_16x16x32_bf16 v[160:163], v[100:103], v[10:13], v[160:163]
	v_min_f32_e32 v173, 0x42fe0000, v173
	v_bfi_b32 v170, s10, v170, v192
	v_bfi_b32 v171, s10, v171, v193
	v_bfi_b32 v172, s10, v172, v194
	v_bfi_b32 v173, s10, v173, v195
	v_cvt_i32_f32_e32 v170, v170
	v_mfma_f32_16x16x32_bf16 v[164:167], v[100:103], v[2:5], v[164:167]
	v_cvt_i32_f32_e32 v171, v171
	v_cvt_i32_f32_e32 v172, v172
	v_cvt_i32_f32_e32 v173, v173
	v_lshl_add_u32 v170, v170, 2, v40
	v_lshl_add_u32 v171, v171, 2, v40
	v_lshl_add_u32 v172, v172, 2, v40
	v_lshl_add_u32 v173, v173, 2, v40
	ds_add_u32 v170, v245 offset:33280
	ds_add_u32 v171, v245 offset:33280
	ds_add_u32 v172, v245 offset:33280
	ds_add_u32 v173, v245 offset:33280
	s_cmp_eq_u32 s100, 0
	s_cbranch_scc0 .Lp1_st_a
	s_waitcnt vmcnt(2)
.Lp1_st_a:
	s_mov_b32 s100, 1
	s_mov_b64 s[0:1], 0
.LBB0_506:
	s_and_b64 vcc, exec, s[0:1]
	s_cbranch_vccz .LBB0_499
	s_cmp_eq_u32 s100, 0
	s_cbranch_scc1 .Lp1_nofl_a
	v_med3_f32 v170, v136, v45, v50
	v_med3_f32 v178, v140, v51, v56
	v_med3_f32 v171, v144, v53, v57
	v_med3_f32 v179, v148, v55, v58
	v_med3_f32 v172, v137, v45, v50
	v_med3_f32 v180, v141, v51, v56
	v_med3_f32 v173, v145, v53, v57
	v_med3_f32 v181, v149, v55, v58
	v_med3_f32 v174, v138, v45, v50
	v_med3_f32 v182, v142, v51, v56
	v_med3_f32 v175, v146, v53, v57
	v_med3_f32 v183, v150, v55, v58
	v_med3_f32 v176, v139, v45, v50
	v_med3_f32 v184, v143, v51, v56
	v_med3_f32 v177, v147, v53, v57
	v_med3_f32 v185, v151, v55, v58
	v_pk_add_f32 v[170:171], v[170:171], v[178:179]
	v_pk_add_f32 v[172:173], v[172:173], v[180:181]
	v_pk_add_f32 v[174:175], v[174:175], v[182:183]
	v_pk_add_f32 v[176:177], v[176:177], v[184:185]
	v_add_f32_e32 v186, v170, v171
	v_add_f32_e32 v187, v172, v173
	v_add_f32_e32 v188, v174, v175
	v_add_f32_e32 v189, v176, v177
	v_cvt_pkrtz_f16_f32 v190, v186, v187
	v_cvt_pkrtz_f16_f32 v191, v188, v189
	global_store_dwordx2 v[208:209], v[190:191], off offset:1024
	v_cvt_f32_f16_e32 v192, v190
	v_cvt_f32_f16_sdwa v193, v190 dst_sel:DWORD dst_unused:UNUSED_PAD src0_sel:WORD_1
	v_cvt_f32_f16_e32 v194, v191
	v_cvt_f32_f16_sdwa v195, v191 dst_sel:DWORD dst_unused:UNUSED_PAD src0_sel:WORD_1
	v_sqrt_f32_e64 v170, |v192|
	v_sqrt_f32_e64 v171, |v193|
	v_sqrt_f32_e64 v172, |v194|
	v_sqrt_f32_e64 v173, |v195|
	v_ceil_f32_e32 v170, v170
	v_ceil_f32_e32 v171, v171
	v_ceil_f32_e32 v172, v172
	v_ceil_f32_e32 v173, v173
	v_min_f32_e32 v170, 0x42fe0000, v170
	v_min_f32_e32 v171, 0x42fe0000, v171
	v_min_f32_e32 v172, 0x42fe0000, v172
	v_min_f32_e32 v173, 0x42fe0000, v173
	v_bfi_b32 v170, s10, v170, v192
	v_bfi_b32 v171, s10, v171, v193
	v_bfi_b32 v172, s10, v172, v194
	v_bfi_b32 v173, s10, v173, v195
	v_cvt_i32_f32_e32 v170, v170
	v_cvt_i32_f32_e32 v171, v171
	v_cvt_i32_f32_e32 v172, v172
	v_cvt_i32_f32_e32 v173, v173
	v_lshl_add_u32 v170, v170, 2, v40
	v_lshl_add_u32 v171, v171, 2, v40
	v_lshl_add_u32 v172, v172, 2, v40
	v_lshl_add_u32 v173, v173, 2, v40
	ds_add_u32 v170, v245 offset:33280
	ds_add_u32 v171, v245 offset:33280
	ds_add_u32 v172, v245 offset:33280
	ds_add_u32 v173, v245 offset:33280
	v_med3_f32 v170, v152, v45, v50
	v_med3_f32 v178, v156, v51, v56
	v_med3_f32 v171, v160, v53, v57
	v_med3_f32 v179, v164, v55, v58
	v_med3_f32 v172, v153, v45, v50
	v_med3_f32 v180, v157, v51, v56
	v_med3_f32 v173, v161, v53, v57
	v_med3_f32 v181, v165, v55, v58
	v_med3_f32 v174, v154, v45, v50
	v_med3_f32 v182, v158, v51, v56
	v_med3_f32 v175, v162, v53, v57
	v_med3_f32 v183, v166, v55, v58
	v_med3_f32 v176, v155, v45, v50
	v_med3_f32 v184, v159, v51, v56
	v_med3_f32 v177, v163, v53, v57
	v_med3_f32 v185, v167, v55, v58
	v_pk_add_f32 v[170:171], v[170:171], v[178:179]
	v_pk_add_f32 v[172:173], v[172:173], v[180:181]
	v_pk_add_f32 v[174:175], v[174:175], v[182:183]
	v_pk_add_f32 v[176:177], v[176:177], v[184:185]
	v_add_f32_e32 v186, v170, v171
	v_add_f32_e32 v187, v172, v173
	v_add_f32_e32 v188, v174, v175
	v_add_f32_e32 v189, v176, v177
	v_cvt_pkrtz_f16_f32 v190, v186, v187
	v_cvt_pkrtz_f16_f32 v191, v188, v189
	global_store_dwordx2 v[208:209], v[190:191], off offset:1536
	v_cvt_f32_f16_e32 v192, v190
	v_cvt_f32_f16_sdwa v193, v190 dst_sel:DWORD dst_unused:UNUSED_PAD src0_sel:WORD_1
	v_cvt_f32_f16_e32 v194, v191
	v_cvt_f32_f16_sdwa v195, v191 dst_sel:DWORD dst_unused:UNUSED_PAD src0_sel:WORD_1
	v_sqrt_f32_e64 v170, |v192|
	v_sqrt_f32_e64 v171, |v193|
	v_sqrt_f32_e64 v172, |v194|
	v_sqrt_f32_e64 v173, |v195|
	v_ceil_f32_e32 v170, v170
	v_ceil_f32_e32 v171, v171
	v_ceil_f32_e32 v172, v172
	v_ceil_f32_e32 v173, v173
	v_min_f32_e32 v170, 0x42fe0000, v170
	v_min_f32_e32 v171, 0x42fe0000, v171
	v_min_f32_e32 v172, 0x42fe0000, v172
	v_min_f32_e32 v173, 0x42fe0000, v173
	v_bfi_b32 v170, s10, v170, v192
	v_bfi_b32 v171, s10, v171, v193
	v_bfi_b32 v172, s10, v172, v194
	v_bfi_b32 v173, s10, v173, v195
	v_cvt_i32_f32_e32 v170, v170
	v_cvt_i32_f32_e32 v171, v171
	v_cvt_i32_f32_e32 v172, v172
	v_cvt_i32_f32_e32 v173, v173
	v_lshl_add_u32 v170, v170, 2, v40
	v_lshl_add_u32 v171, v171, 2, v40
	v_lshl_add_u32 v172, v172, 2, v40
	v_lshl_add_u32 v173, v173, 2, v40
	ds_add_u32 v170, v245 offset:33280
	ds_add_u32 v171, v245 offset:33280
	ds_add_u32 v172, v245 offset:33280
	ds_add_u32 v173, v245 offset:33280
	s_mov_b32 s100, 0
.Lp1_nofl_a:
	s_mov_b32 s0, 0
	v_mov_b64_e32 v[38:39], v[36:37]
